# attention phase: waves 0-3 raised to priority 2 (one wave per SIMD) so the two waves of a SIMD fall out of lockstep; priority back to 0 at the next phase
# baseline (speedup 1.0000x reference)
.LBB0_2639:
	s_cmp_lt_i32 s56, 12
	s_cselect_b64 s[0:1], -1, 0
	s_cmp_gt_i32 s57, 11
	s_cselect_b64 s[2:3], -1, 0
	s_and_b64 s[0:1], s[0:1], s[2:3]
	s_andn2_b64 vcc, exec, s[0:1]
	s_cbranch_vccnz .LBB0_3508
	v_readfirstlane_b32 s98, v0
	s_bitcmp1_b32 s98, 8
	s_cbranch_scc1 .Lattn_lo
	s_setprio 2
.Lattn_lo:
	s_and_b32 s0, s86, 7
	s_mul_i32 s0, s0, 3
	s_mov_b32 s0, 0
	s_add_u32 s1, s96, 0x3ea00000
	v_writelane_b32 v255, s1, 11
	s_addc_u32 s1, s97, 0
	v_writelane_b32 v255, s1, 12
	s_add_u32 s1, s96, 0x4aa00000
	v_readlane_b32 s4, v254, 7
	v_writelane_b32 v255, s1, 13
	s_addc_u32 s1, s97, 0
	s_ashr_i32 s3, s4, 31
	s_mul_i32 s2, s94, s0
	v_writelane_b32 v255, s1, 14
	s_mul_hi_i32 s1, s94, s0
	s_add_u32 s0, s2, s4
	s_addc_u32 s1, s1, s3
	s_waitcnt vmcnt(0)
	v_mov_b64_e32 v[2:3], 0x200
	v_mov_b32_e32 v1, v0
	v_writelane_b32 v255, s2, 15
	v_cmp_lt_i64_e32 vcc, s[0:1], v[2:3]
	v_writelane_b32 v255, s3, 16
	s_and_b64 s[2:3], vcc, exec
	s_cselect_b32 s0, s0, 0x200
	v_bfe_u32 v1, v0, 5, 1
	v_writelane_b32 v255, s0, 17
	s_cmp_ge_i32 s4, s0
	v_and_b32_e32 v182, 31, v0
	v_lshlrev_b32_e32 v199, 3, v0
	v_and_b32_e32 v196, 63, v0
	v_lshlrev_b32_e32 v185, 2, v1
	v_lshlrev_b32_e32 v184, 3, v1
	v_lshlrev_b32_e32 v198, 4, v1
	v_and_b32_e32 v197, 3, v0
	v_lshlrev_b32_e32 v186, 13, v1
	s_cbranch_scc1 .LBB0_2890
	v_readlane_b32 s74, v254, 7
	s_ashr_i32 s2, s74, 6
	s_ashr_i32 s3, s2, 31
	s_lshl_b32 s1, s74, 8
	s_lshl_b64 s[4:5], s[2:3], 11
	s_and_b32 s24, s1, 0x300
	s_or_b32 s4, s4, s24
	s_mul_i32 s1, s5, 0x3000
	s_mul_hi_u32 s3, s4, 0x3000
	s_ashr_i32 s0, s74, 2
	s_add_i32 s3, s3, s1
	s_mul_i32 s1, s4, 0x3000
	v_readlane_b32 s8, v255, 11
	s_add_u32 s1, s8, s1
	v_readlane_b32 s9, v255, 12
	s_addc_u32 s3, s9, s3
	s_lshl_b32 s6, s0, 7
	s_and_b32 s6, s6, 0x780
	s_lshl_b32 s7, s6, 1
	s_add_u32 s10, s1, s7
	s_addc_u32 s11, s3, 0
	s_mul_hi_i32 s1, s2, 0x1800000
	s_mul_i32 s2, s2, 0x1800000
	s_add_u32 s2, s8, s2
	s_addc_u32 s1, s9, s1
	s_add_u32 s2, s2, s7
	s_addc_u32 s1, s1, 0
	s_add_u32 s70, s2, 0x1000
	s_addc_u32 s71, s1, 0
	s_add_u32 s90, s2, 0x2000
	s_addc_u32 s91, s1, 0
	s_lshl_b64 s[2:3], s[4:5], 11
	v_readlane_b32 s1, v255, 13
	s_add_u32 s1, s1, s2
	v_readlane_b32 s2, v255, 14
	s_addc_u32 s2, s2, s3
	s_add_u32 s88, s1, s6
	s_addc_u32 s89, s2, 0
	s_ashr_i32 s1, s0, 31
	s_lshl_b64 s[0:1], s[0:1], 12
	v_readlane_b32 s2, v255, 7
	v_readlane_b32 s3, v255, 8
	s_add_u32 s8, s2, s0
	v_readfirstlane_b32 s0, v0
	s_addc_u32 s9, s3, s1
	s_lshr_b32 s2, s0, 6
	s_movk_i32 s33, 0x3000
	v_lshl_or_b32 v1, s2, 5, v182
	v_writelane_b32 v255, s10, 18
	v_and_b32_e32 v20, 0x78, v199
	v_lshlrev_b32_e32 v22, 1, v20
	v_mov_b64_e32 v[2:3], s[10:11]
	v_mad_u64_u32 v[4:5], s[0:1], v1, s33, v[2:3]
	v_or_b32_e32 v1, s24, v227
	v_and_b32_e32 v2, 16, v226
	v_mov_b32_e32 v3, 0
	v_mul_u32_u24_e32 v1, 0x1800, v1
	v_lshl_add_u64 v[4:5], v[4:5], 0, v[2:3]
	v_lshlrev_b32_e32 v2, 1, v1
	v_or_b32_e32 v1, 32, v227
	v_or_b32_e32 v6, s24, v1
	v_mul_u32_u24_e32 v6, 0x1800, v6
	v_mov_b32_e32 v23, v3
	v_lshlrev_b32_e32 v6, 1, v6
	v_mov_b32_e32 v7, v3
	v_lshl_add_u64 v[8:9], s[70:71], 0, v[2:3]
	v_lshl_add_u64 v[8:9], v[8:9], 0, v[22:23]
	v_lshl_add_u64 v[10:11], s[70:71], 0, v[6:7]
	v_lshl_add_u64 v[10:11], v[10:11], 0, v[22:23]
	global_load_dwordx4 v[12:15], v[8:9], off
	global_load_dwordx4 v[16:19], v[10:11], off
	s_lshl_b32 s0, s2, 13
	s_add_i32 s0, s0, 0
	s_add_i32 m0, s0, 0x10840
	v_lshl_add_u64 v[8:9], v[4:5], 0, 32
	global_load_lds_dwordx4 v[4:5], off
	s_add_i32 m0, s0, 0x10c40
	s_mov_b64 s[2:3], 0x60
	global_load_lds_dwordx4 v[8:9], off
	v_lshl_add_u64 v[8:9], v[4:5], 0, 64
	s_add_i32 m0, s0, 0x11040
	v_lshl_add_u64 v[6:7], s[90:91], 0, v[6:7]
	global_load_lds_dwordx4 v[8:9], off
	v_lshl_add_u64 v[8:9], v[4:5], 0, s[2:3]
	s_add_i32 m0, s0, 0x11440
	s_mov_b64 s[2:3], 0x80
	global_load_lds_dwordx4 v[8:9], off
	v_lshl_add_u64 v[8:9], v[4:5], 0, s[2:3]
	s_add_i32 m0, s0, 0x11840
	s_mov_b64 s[2:3], 0xa0
	global_load_lds_dwordx4 v[8:9], off
	v_lshl_add_u64 v[8:9], v[4:5], 0, s[2:3]
	s_add_i32 m0, s0, 0x11c40
	s_mov_b64 s[2:3], 0xc0
	global_load_lds_dwordx4 v[8:9], off
	v_lshl_add_u64 v[8:9], v[4:5], 0, s[2:3]
	s_add_i32 m0, s0, 0x12040
	s_mov_b64 s[2:3], 0xe0
	global_load_lds_dwordx4 v[8:9], off
	v_lshl_add_u64 v[4:5], v[4:5], 0, s[2:3]
	s_add_i32 m0, s0, 0x12440
	v_lshl_add_u64 v[8:9], v[6:7], 0, v[22:23]
	global_load_lds_dwordx4 v[4:5], off
	v_lshl_add_u64 v[4:5], s[90:91], 0, v[2:3]
	v_lshl_add_u64 v[4:5], v[4:5], 0, v[22:23]
	global_load_dwordx4 v[4:7], v[4:5], off
	s_nop 0
	global_load_dwordx4 v[8:11], v[8:9], off
	s_movk_i32 s0, 0x70
	v_lshlrev_b32_e32 v2, 8, v227
	v_bitop3_b32 v23, v22, v0, s0 bitop3:0x78
	v_add3_u32 v23, 0, v2, v23
	s_waitcnt vmcnt(0)
	s_waitcnt vmcnt(0)
	ds_write_b128 v23, v[12:15] offset:32768
	ds_write_b128 v23, v[16:19] offset:40960
	v_lshrrev_b32_e32 v12, 3, v0
	v_and_b32_e32 v12, 8, v12
	v_and_or_b32 v13, v227, 16, v12
	v_and_or_b32 v12, v1, 48, v12
	v_lshrrev_b32_e32 v13, 1, v13
	v_bfe_u32 v14, v199, 5, 2
	v_lshrrev_b32_e32 v15, 5, v0
	v_lshrrev_b32_e32 v12, 1, v12
	v_or_b32_e32 v13, v13, v14
	v_and_or_b32 v15, v15, 4, v223
	v_or_b32_e32 v12, v12, v14
	v_writelane_b32 v255, s11, 19
	v_lshlrev_b32_e32 v13, 9, v13
	v_lshlrev_b32_e32 v15, 6, v15
	v_and_b32_e32 v16, 48, v22
	v_lshlrev_b32_e32 v12, 9, v12
	v_lshlrev_b32_e32 v201, 4, v196
	v_cmp_eq_u32_e64 s[2:3], 0, v196
	v_or3_b32 v13, v13, v15, v16
	v_or3_b32 v12, v12, v15, v16
	v_and_b32_e32 v14, 0xc0, v201
	v_and_b32_e32 v15, 32, v225
	v_and_b32_e32 v16, 0x118, v199
	v_writelane_b32 v255, s2, 20
	v_or3_b32 v14, v16, v15, v14
	v_bitop3_b32 v16, v198, v249, s0 bitop3:0x78
	v_writelane_b32 v255, s3, 21
	s_add_i32 s0, 0, 0x10810
	v_writelane_b32 v255, s0, 22
	v_writelane_b32 v255, s8, 23
	v_and_b32_e32 v21, 0x70, v0
	s_movk_i32 s1, 0x60
	v_writelane_b32 v255, s9, 24
	v_writelane_b32 v255, s88, 25
	v_add_u32_e32 v204, 0, v14
	v_and_b32_e32 v14, 0x70, v249
	v_writelane_b32 v255, s89, 26
	v_bitop3_b32 v2, v22, v2, v21 bitop3:0xde
	v_lshl_add_u32 v15, v182, 8, 0
	v_bitop3_b32 v17, v198, v14, 32 bitop3:0x36
	v_bitop3_b32 v19, v198, v14, 64 bitop3:0x36
	v_bitop3_b32 v14, v198, v14, s1 bitop3:0x36
	v_writelane_b32 v255, s70, 9
	s_mov_b32 s73, 0
	v_sub_u32_e32 v200, v182, v185
	v_or_b32_e32 v202, 64, v227
	v_or_b32_e32 v203, 0x60, v227
	v_cmp_gt_u32_e64 s[4:5], 32, v196
	v_cmp_eq_u32_e64 s[6:7], 0, v197
	v_mov_b32_e32 v183, v3
	v_mov_b32_e32 v187, v3
	s_mov_b32 s1, 0x41000000
	v_lshlrev_b32_e32 v188, 1, v20
	s_mov_b32 s0, 0x3e0293ee
	v_lshlrev_b32_e32 v190, 1, v184
	s_mov_b32 s92, 0xc3e00000
	v_add_u32_e32 v205, 0, v13
	v_add_u32_e32 v206, 0, v12
	v_mov_b32_e32 v18, 0xff800000
	v_add_u32_e32 v207, v15, v16
	v_add_u32_e32 v208, v15, v17
	v_add_u32_e32 v209, v15, v19
	v_add_u32_e32 v210, v15, v14
	v_add_u32_e32 v211, 0, v2
	v_mov_b32_e32 v212, 0xf149f2ca
	v_mov_b32_e32 v213, 0x43e00000
	s_mov_b32 s93, 0
	s_mov_b32 s75, s24
	s_mov_b64 s[78:79], s[90:91]
	v_writelane_b32 v255, s71, 10
	s_waitcnt lgkmcnt(0)
	s_barrier
	s_branch .LBB0_2643

.LBB0_3508:
	s_setprio 0
	s_cmp_lt_i32 s56, 13
	s_cselect_b64 s[0:1], -1, 0
	s_cmp_gt_i32 s57, 12
	s_cselect_b64 s[2:3], -1, 0
	s_and_b64 s[0:1], s[0:1], s[2:3]
	s_andn2_b64 vcc, exec, s[0:1]
	s_cbranch_vccnz .LBB0_3591
	s_waitcnt vmcnt(0)
	v_mov_b32_e32 v1, v0
	s_cmpk_gt_i32 s86, 0x1ff
	v_readfirstlane_b32 s6, v0
	s_cbranch_scc1 .LBB0_3541
	s_ashr_i32 s9, s86, 31
	s_lshr_b32 s0, s9, 29
	s_add_i32 s2, s86, s0
	s_and_b32 s0, s2, -8
	s_sub_i32 s4, s86, s0
	s_cmp_gt_i32 s4, -1
	s_cbranch_scc0 .LBB0_3512
	s_lshl_b32 s3, s4, 6
	s_cbranch_execz .LBB0_3513
	s_branch .LBB0_3514
